# instruction selection: P2 streamer x64 scale via 4 v_pk_mul_f32 (in MMA4 nop slots) instead of 8 v_mul_f32 (4 fewer inserted issue slots per iteration)
# baseline (speedup 1.0000x reference)
.Lp2_top:
	ds_read_b128 v[158:161], v217
	ds_read_b128 v[162:165], v218
	ds_read_b128 v[166:169], v219
	ds_read_b128 v[170:173], v220
	ds_read_b128 v[148:151], v221
	ds_read_b128 v[144:147], v222
	ds_read_b128 v[140:143], v223
	ds_read_b128 v[136:139], v224
	ds_read_b128 v[174:177], v233
	ds_read_b128 v[178:181], v233 offset:1024
	ds_read_b128 v[182:185], v233 offset:2048
	ds_read_b128 v[186:189], v233 offset:3072
	ds_read_b128 v[190:193], v233 offset:4096
	ds_read_b128 v[194:197], v233 offset:5120
	ds_read_b128 v[234:237], v233 offset:6144
	ds_read_b128 v[238:241], v233 offset:7168
	s_add_i32 s4, s60, s61
	s_mov_b32 s46, s94
	s_add_i32 s94, s94, 1
	s_add_i32 s5, s4, 0x200
	s_add_i32 s16, s33, s61
	s_cmpk_eq_i32 s61, 0x1e00
	s_cselect_b32 s47, s90, s5
	s_cselect_b32 s97, s91, s16
	s_add_i32 s96, s47, 0x80
	s_mov_b32 m0, s82
	s_add_i32 s5, s4, 0x100180
	buffer_load_dwordx4 v214, s[8:11], s5 offen lds
	s_add_i32 s4, s4, 0x180180
	s_mov_b32 m0, s85
	s_add_i32 vcc_lo, s97, 0x80
	buffer_load_dwordx4 v214, s[8:11], s4 offen lds
	s_lshr_b32 s4, s94, 2
	s_mul_i32 s5, s4, s34
	s_add_i32 s16, s5, s2
	s_cmp_lt_i32 s4, s3
	s_cselect_b64 s[4:5], -1, 0
	s_and_b64 s[44:45], s[4:5], exec
	s_cselect_b32 s16, s16, 0
	s_bfe_u32 s17, s94, 0x10001
	s_or_b32 s17, s17, s83
	s_bfe_u32 s67, s16, 0x50007
	s_bfe_u32 s36, s16, 0x50002
	s_and_b32 s95, s16, 3
	s_cmpk_gt_i32 s16, 0xfff
	s_cselect_b64 s[44:45], -1, 0
	v_lshl_or_b32 v156, s17, 3, v216
	s_and_b64 s[16:17], s[44:45], exec
	s_cselect_b32 s16, s25, s21
	s_cselect_b32 s17, s24, s20
	s_lshl_b32 vcc_hi, s67, 23
	s_add_u32 s17, s17, vcc_hi
	s_addc_u32 s16, s16, 0
	s_lshl_b32 vcc_hi, s36, 18
	s_add_u32 s17, s17, vcc_hi
	s_addc_u32 vcc_hi, s16, 0
	s_lshl_b32 s16, s95, 9
	s_add_u32 s16, s17, s16
	v_and_or_b32 v204, s66, 2, v200
	s_addc_u32 s17, vcc_hi, 0
	v_lshlrev_b64 v[128:129], 11, v[204:205]
	v_lshl_add_u64 v[128:129], s[16:17], 0, v[128:129]
	v_lshlrev_b32_e32 v204, 4, v156
	v_lshl_add_u64 v[132:133], v[128:129], 0, v[204:205]
	global_load_dwordx4 v[128:131], v[132:133], off nt
	s_nop 0
	global_load_dwordx4 v[132:135], v[132:133], off offset:2048 nt
	s_waitcnt vmcnt(10)
	s_waitcnt lgkmcnt(8)
	s_barrier
	s_setprio 1
	s_waitcnt lgkmcnt(7)
	v_mfma_f32_16x16x32_bf16 v[124:127], v[158:161], v[174:177], v[124:127]
	s_waitcnt lgkmcnt(6)
	v_mfma_f32_16x16x32_bf16 v[124:127], v[162:165], v[178:181], v[124:127]
	v_mfma_f32_16x16x32_bf16 v[120:123], v[166:169], v[174:177], v[120:123]
	s_nop 0
	v_mfma_f32_16x16x32_bf16 v[120:123], v[170:173], v[178:181], v[120:123]
	s_waitcnt lgkmcnt(5)
	v_mfma_f32_16x16x32_bf16 v[116:119], v[158:161], v[182:185], v[116:119]
	s_waitcnt lgkmcnt(4)
	v_mfma_f32_16x16x32_bf16 v[116:119], v[162:165], v[186:189], v[116:119]
	v_mfma_f32_16x16x32_bf16 v[112:115], v[166:169], v[182:185], v[112:115]
	s_nop 0
	v_mfma_f32_16x16x32_bf16 v[112:115], v[170:173], v[186:189], v[112:115]
	s_waitcnt lgkmcnt(3)
	v_mfma_f32_16x16x32_bf16 v[108:111], v[158:161], v[190:193], v[108:111]
	s_waitcnt lgkmcnt(2)
	v_mfma_f32_16x16x32_bf16 v[108:111], v[162:165], v[194:197], v[108:111]
	v_mfma_f32_16x16x32_bf16 v[104:107], v[166:169], v[190:193], v[104:107]
	s_nop 0
	v_mfma_f32_16x16x32_bf16 v[104:107], v[170:173], v[194:197], v[104:107]
	s_waitcnt lgkmcnt(1)
	v_mfma_f32_16x16x32_bf16 v[100:103], v[158:161], v[234:237], v[100:103]
	s_waitcnt lgkmcnt(0)
	v_mfma_f32_16x16x32_bf16 v[100:103], v[162:165], v[238:241], v[100:103]
	v_mfma_f32_16x16x32_bf16 v[96:99], v[166:169], v[234:237], v[96:99]
	s_nop 0
	v_mfma_f32_16x16x32_bf16 v[96:99], v[170:173], v[238:241], v[96:99]
	s_setprio 0
	s_setprio 1
	v_mfma_f32_16x16x32_bf16 v[92:95], v[148:151], v[174:177], v[92:95]
	s_nop 0
	v_mfma_f32_16x16x32_bf16 v[92:95], v[144:147], v[178:181], v[92:95]
	v_mfma_f32_16x16x32_bf16 v[88:91], v[140:143], v[174:177], v[88:91]
	s_nop 0
	v_mfma_f32_16x16x32_bf16 v[88:91], v[136:139], v[178:181], v[88:91]
	v_mfma_f32_16x16x32_bf16 v[84:87], v[148:151], v[182:185], v[84:87]
	s_nop 0
	v_mfma_f32_16x16x32_bf16 v[84:87], v[144:147], v[186:189], v[84:87]
	v_mfma_f32_16x16x32_bf16 v[80:83], v[140:143], v[182:185], v[80:83]
	s_nop 0
	v_mfma_f32_16x16x32_bf16 v[80:83], v[136:139], v[186:189], v[80:83]
	v_mfma_f32_16x16x32_bf16 v[76:79], v[148:151], v[190:193], v[76:79]
	s_nop 0
	v_mfma_f32_16x16x32_bf16 v[76:79], v[144:147], v[194:197], v[76:79]
	v_mfma_f32_16x16x32_bf16 v[72:75], v[140:143], v[190:193], v[72:75]
	s_nop 0
	v_mfma_f32_16x16x32_bf16 v[72:75], v[136:139], v[194:197], v[72:75]
	v_mfma_f32_16x16x32_bf16 v[68:71], v[148:151], v[234:237], v[68:71]
	s_nop 0
	v_mfma_f32_16x16x32_bf16 v[68:71], v[144:147], v[238:241], v[68:71]
	v_mfma_f32_16x16x32_bf16 v[64:67], v[140:143], v[234:237], v[64:67]
	s_nop 0
	v_mfma_f32_16x16x32_bf16 v[64:67], v[136:139], v[238:241], v[64:67]
	s_setprio 0
	s_barrier
	ds_read_b128 v[174:177], v233 offset:16384
	ds_read_b128 v[178:181], v233 offset:17408
	ds_read_b128 v[182:185], v233 offset:18432
	ds_read_b128 v[186:189], v233 offset:19456
	ds_read_b128 v[190:193], v233 offset:20480
	ds_read_b128 v[194:197], v233 offset:21504
	ds_read_b128 v[234:237], v233 offset:22528
	ds_read_b128 v[238:241], v233 offset:23552
	s_mov_b32 m0, s65
	s_add_i32 s16, s97, 0x100000
	buffer_load_dwordx4 v215, s[12:15], s97 offen lds
	s_mov_b32 m0, s68
	s_nop 0
	buffer_load_dwordx4 v215, s[12:15], s16 offen lds
	s_add_i32 s16, s97, 0x10000
	s_mov_b32 m0, s69
	s_nop 0
	buffer_load_dwordx4 v215, s[12:15], s16 offen lds
	s_add_i32 s16, s97, 0x110000
	s_mov_b32 m0, s70
	s_nop 0
	buffer_load_dwordx4 v215, s[12:15], s16 offen lds
	s_mov_b32 m0, s64
	s_add_i32 s16, s47, 0x80000
	buffer_load_dwordx4 v214, s[8:11], s47 offen lds
	s_mov_b32 m0, s71
	s_nop 0
	buffer_load_dwordx4 v214, s[8:11], s16 offen lds
	s_waitcnt vmcnt(10)
	s_waitcnt lgkmcnt(6)
	s_barrier
	s_setprio 1
	s_waitcnt lgkmcnt(7)
	v_mfma_f32_16x16x32_bf16 v[60:63], v[158:161], v[174:177], v[60:63]
	s_waitcnt lgkmcnt(6)
	v_mfma_f32_16x16x32_bf16 v[60:63], v[162:165], v[178:181], v[60:63]
	v_mfma_f32_16x16x32_bf16 v[56:59], v[166:169], v[174:177], v[56:59]
	s_nop 0
	v_mfma_f32_16x16x32_bf16 v[56:59], v[170:173], v[178:181], v[56:59]
	s_waitcnt lgkmcnt(5)
	v_mfma_f32_16x16x32_bf16 v[52:55], v[158:161], v[182:185], v[52:55]
	s_waitcnt lgkmcnt(4)
	v_mfma_f32_16x16x32_bf16 v[52:55], v[162:165], v[186:189], v[52:55]
	v_mfma_f32_16x16x32_bf16 v[48:51], v[166:169], v[182:185], v[48:51]
	s_nop 0
	v_mfma_f32_16x16x32_bf16 v[48:51], v[170:173], v[186:189], v[48:51]
	s_waitcnt lgkmcnt(3)
	v_mfma_f32_16x16x32_bf16 v[44:47], v[158:161], v[190:193], v[44:47]
	s_waitcnt lgkmcnt(2)
	v_mfma_f32_16x16x32_bf16 v[44:47], v[162:165], v[194:197], v[44:47]
	v_mfma_f32_16x16x32_bf16 v[40:43], v[166:169], v[190:193], v[40:43]
	s_nop 0
	v_mfma_f32_16x16x32_bf16 v[40:43], v[170:173], v[194:197], v[40:43]
	s_waitcnt lgkmcnt(1)
	v_mfma_f32_16x16x32_bf16 v[36:39], v[158:161], v[234:237], v[36:39]
	s_waitcnt lgkmcnt(0)
	v_mfma_f32_16x16x32_bf16 v[36:39], v[162:165], v[238:241], v[36:39]
	v_mfma_f32_16x16x32_bf16 v[32:35], v[166:169], v[234:237], v[32:35]
	s_nop 0
	v_mfma_f32_16x16x32_bf16 v[32:35], v[170:173], v[238:241], v[32:35]
	s_setprio 0
	s_setprio 1
	v_mfma_f32_16x16x32_bf16 v[28:31], v[148:151], v[174:177], v[28:31]
	s_nop 0
	v_mfma_f32_16x16x32_bf16 v[28:31], v[144:147], v[178:181], v[28:31]
	v_mfma_f32_16x16x32_bf16 v[24:27], v[140:143], v[174:177], v[24:27]
	s_nop 0
	v_mfma_f32_16x16x32_bf16 v[24:27], v[136:139], v[178:181], v[24:27]
	v_mfma_f32_16x16x32_bf16 v[20:23], v[148:151], v[182:185], v[20:23]
	s_nop 0
	v_mfma_f32_16x16x32_bf16 v[20:23], v[144:147], v[186:189], v[20:23]
	v_mfma_f32_16x16x32_bf16 v[16:19], v[140:143], v[182:185], v[16:19]
	s_nop 0
	v_mfma_f32_16x16x32_bf16 v[16:19], v[136:139], v[186:189], v[16:19]
	v_mfma_f32_16x16x32_bf16 v[12:15], v[148:151], v[190:193], v[12:15]
	s_nop 0
	v_mfma_f32_16x16x32_bf16 v[12:15], v[144:147], v[194:197], v[12:15]
	v_mfma_f32_16x16x32_bf16 v[8:11], v[140:143], v[190:193], v[8:11]
	s_nop 0
	v_mfma_f32_16x16x32_bf16 v[8:11], v[136:139], v[194:197], v[8:11]
	v_mfma_f32_16x16x32_bf16 v[4:7], v[148:151], v[234:237], v[4:7]
	s_nop 0
	v_mfma_f32_16x16x32_bf16 v[4:7], v[144:147], v[238:241], v[4:7]
	v_mfma_f32_16x16x32_bf16 v[0:3], v[140:143], v[234:237], v[0:3]
	s_nop 0
	v_mfma_f32_16x16x32_bf16 v[0:3], v[136:139], v[238:241], v[0:3]
	s_setprio 0
	s_barrier
	ds_read_b128 v[136:139], v225
	ds_read_b128 v[140:143], v226
	ds_read_b128 v[144:147], v227
	ds_read_b128 v[148:151], v228
	ds_read_b128 v[158:161], v229
	ds_read_b128 v[162:165], v230
	ds_read_b128 v[166:169], v231
	ds_read_b128 v[170:173], v232
	ds_read_b128 v[174:177], v233 offset:32768
	ds_read_b128 v[178:181], v233 offset:33792
	ds_read_b128 v[182:185], v233 offset:34816
	ds_read_b128 v[186:189], v233 offset:35840
	ds_read_b128 v[190:193], v233 offset:36864
	ds_read_b128 v[194:197], v233 offset:37888
	ds_read_b128 v[234:237], v233 offset:38912
	ds_read_b128 v[238:241], v233 offset:39936
	s_mov_b32 m0, s72
	s_add_i32 s16, s47, 0x100000
	buffer_load_dwordx4 v214, s[8:11], s16 offen lds
	s_add_i32 s16, s47, 0x180000
	s_mov_b32 m0, s73
	s_nop 0
	buffer_load_dwordx4 v214, s[8:11], s16 offen lds
	s_waitcnt vmcnt(10)
	s_waitcnt lgkmcnt(8)
	s_barrier
	s_setprio 1
	s_waitcnt lgkmcnt(7)
	v_mfma_f32_16x16x32_bf16 v[124:127], v[136:139], v[174:177], v[124:127]
	s_waitcnt lgkmcnt(6)
	v_mfma_f32_16x16x32_bf16 v[124:127], v[140:143], v[178:181], v[124:127]
	v_mfma_f32_16x16x32_bf16 v[120:123], v[144:147], v[174:177], v[120:123]
	s_nop 0
	v_mfma_f32_16x16x32_bf16 v[120:123], v[148:151], v[178:181], v[120:123]
	s_waitcnt lgkmcnt(5)
	v_mfma_f32_16x16x32_bf16 v[116:119], v[136:139], v[182:185], v[116:119]
	s_waitcnt lgkmcnt(4)
	v_mfma_f32_16x16x32_bf16 v[116:119], v[140:143], v[186:189], v[116:119]
	v_mfma_f32_16x16x32_bf16 v[112:115], v[144:147], v[182:185], v[112:115]
	s_nop 0
	v_mfma_f32_16x16x32_bf16 v[112:115], v[148:151], v[186:189], v[112:115]
	s_waitcnt lgkmcnt(3)
	v_mfma_f32_16x16x32_bf16 v[108:111], v[136:139], v[190:193], v[108:111]
	s_waitcnt lgkmcnt(2)
	v_mfma_f32_16x16x32_bf16 v[108:111], v[140:143], v[194:197], v[108:111]
	v_mfma_f32_16x16x32_bf16 v[104:107], v[144:147], v[190:193], v[104:107]
	s_nop 0
	v_mfma_f32_16x16x32_bf16 v[104:107], v[148:151], v[194:197], v[104:107]
	s_waitcnt lgkmcnt(1)
	v_mfma_f32_16x16x32_bf16 v[100:103], v[136:139], v[234:237], v[100:103]
	s_waitcnt lgkmcnt(0)
	v_mfma_f32_16x16x32_bf16 v[100:103], v[140:143], v[238:241], v[100:103]
	v_mfma_f32_16x16x32_bf16 v[96:99], v[144:147], v[234:237], v[96:99]
	s_nop 0
	v_mfma_f32_16x16x32_bf16 v[96:99], v[148:151], v[238:241], v[96:99]
	s_setprio 0
	s_setprio 1
	v_mfma_f32_16x16x32_bf16 v[92:95], v[158:161], v[174:177], v[92:95]
	s_nop 0
	v_mfma_f32_16x16x32_bf16 v[92:95], v[162:165], v[178:181], v[92:95]
	v_mfma_f32_16x16x32_bf16 v[88:91], v[166:169], v[174:177], v[88:91]
	s_nop 0
	v_mfma_f32_16x16x32_bf16 v[88:91], v[170:173], v[178:181], v[88:91]
	v_mfma_f32_16x16x32_bf16 v[84:87], v[158:161], v[182:185], v[84:87]
	s_nop 0
	v_mfma_f32_16x16x32_bf16 v[84:87], v[162:165], v[186:189], v[84:87]
	v_mfma_f32_16x16x32_bf16 v[80:83], v[166:169], v[182:185], v[80:83]
	s_nop 0
	v_mfma_f32_16x16x32_bf16 v[80:83], v[170:173], v[186:189], v[80:83]
	v_mfma_f32_16x16x32_bf16 v[76:79], v[158:161], v[190:193], v[76:79]
	s_nop 0
	v_mfma_f32_16x16x32_bf16 v[76:79], v[162:165], v[194:197], v[76:79]
	v_mfma_f32_16x16x32_bf16 v[72:75], v[166:169], v[190:193], v[72:75]
	s_nop 0
	v_mfma_f32_16x16x32_bf16 v[72:75], v[170:173], v[194:197], v[72:75]
	v_mfma_f32_16x16x32_bf16 v[68:71], v[158:161], v[234:237], v[68:71]
	s_nop 0
	v_mfma_f32_16x16x32_bf16 v[68:71], v[162:165], v[238:241], v[68:71]
	v_mfma_f32_16x16x32_bf16 v[64:67], v[166:169], v[234:237], v[64:67]
	s_nop 0
	v_mfma_f32_16x16x32_bf16 v[64:67], v[170:173], v[238:241], v[64:67]
	s_setprio 0
	s_barrier
	ds_read_b128 v[174:177], v233 offset:49152
	ds_read_b128 v[178:181], v233 offset:50176
	ds_read_b128 v[182:185], v233 offset:51200
	ds_read_b128 v[186:189], v233 offset:52224
	ds_read_b128 v[190:193], v233 offset:53248
	ds_read_b128 v[194:197], v233 offset:54272
	ds_read_b128 v[234:237], v233 offset:55296
	ds_read_b128 v[238:241], v233 offset:56320
	s_mov_b32 m0, s76
	s_add_i32 s16, s97, 0x100080
	buffer_load_dwordx4 v215, s[12:15], vcc_lo offen lds
	s_mov_b32 m0, s77
	s_add_i32 s47, s47, 0x80080
	buffer_load_dwordx4 v215, s[12:15], s16 offen lds
	s_add_i32 s16, s97, 0x10080
	s_mov_b32 m0, s80
	s_add_i32 s97, s97, 0x110080
	buffer_load_dwordx4 v215, s[12:15], s16 offen lds
	s_mov_b32 m0, s81
	s_nop 0
	buffer_load_dwordx4 v215, s[12:15], s97 offen lds
	s_mov_b32 m0, s78
	s_nop 0
	buffer_load_dwordx4 v214, s[8:11], s96 offen lds
	s_mov_b32 m0, s79
	s_nop 0
	buffer_load_dwordx4 v214, s[8:11], s47 offen lds
	s_bitcmp0_b32 s46, 0
	s_mov_b32 s98, 0xffff
	s_cselect_b32 s98, 0xffff0000, s98
	s_mov_b32 s100, 0x42800000
	s_mov_b32 s101, 0x42800000
	s_waitcnt vmcnt(8)
	s_waitcnt lgkmcnt(6)
	s_barrier
	s_setprio 1
	s_waitcnt lgkmcnt(7)
	v_mfma_f32_16x16x32_bf16 v[60:63], v[136:139], v[174:177], v[60:63]
	s_waitcnt lgkmcnt(6)
	v_mfma_f32_16x16x32_bf16 v[60:63], v[140:143], v[178:181], v[60:63]
	v_mfma_f32_16x16x32_bf16 v[56:59], v[144:147], v[174:177], v[56:59]
	v_pk_mul_f32 v[128:129], v[128:129], s[100:101]
	v_mfma_f32_16x16x32_bf16 v[56:59], v[148:151], v[178:181], v[56:59]
	s_waitcnt lgkmcnt(5)
	v_mfma_f32_16x16x32_bf16 v[52:55], v[136:139], v[182:185], v[52:55]
	s_waitcnt lgkmcnt(4)
	v_mfma_f32_16x16x32_bf16 v[52:55], v[140:143], v[186:189], v[52:55]
	v_mfma_f32_16x16x32_bf16 v[48:51], v[144:147], v[182:185], v[48:51]
	v_pk_mul_f32 v[130:131], v[130:131], s[100:101]
	v_mfma_f32_16x16x32_bf16 v[48:51], v[148:151], v[186:189], v[48:51]
	s_waitcnt lgkmcnt(3)
	v_mfma_f32_16x16x32_bf16 v[44:47], v[136:139], v[190:193], v[44:47]
	s_waitcnt lgkmcnt(2)
	v_mfma_f32_16x16x32_bf16 v[44:47], v[140:143], v[194:197], v[44:47]
	v_mfma_f32_16x16x32_bf16 v[40:43], v[144:147], v[190:193], v[40:43]
	v_pk_mul_f32 v[132:133], v[132:133], s[100:101]
	v_mfma_f32_16x16x32_bf16 v[40:43], v[148:151], v[194:197], v[40:43]
	s_waitcnt lgkmcnt(1)
	v_mfma_f32_16x16x32_bf16 v[36:39], v[136:139], v[234:237], v[36:39]
	s_waitcnt lgkmcnt(0)
	v_mfma_f32_16x16x32_bf16 v[36:39], v[140:143], v[238:241], v[36:39]
	v_mfma_f32_16x16x32_bf16 v[32:35], v[144:147], v[234:237], v[32:35]
	v_pk_mul_f32 v[134:135], v[134:135], s[100:101]
	v_mfma_f32_16x16x32_bf16 v[32:35], v[148:151], v[238:241], v[32:35]
	s_setprio 0
	s_setprio 1
	v_mfma_f32_16x16x32_bf16 v[28:31], v[158:161], v[174:177], v[28:31]
	v_cvt_pk_fp8_f32 v204, v128, v132
	v_mfma_f32_16x16x32_bf16 v[28:31], v[162:165], v[178:181], v[28:31]
	v_mfma_f32_16x16x32_bf16 v[24:27], v[166:169], v[174:177], v[24:27]
	v_cvt_pk_fp8_f32 v204, v128, v132 op_sel:[0,0,1]
	v_mfma_f32_16x16x32_bf16 v[24:27], v[170:173], v[178:181], v[24:27]
	v_mfma_f32_16x16x32_bf16 v[20:23], v[158:161], v[182:185], v[20:23]
	v_cvt_pk_fp8_f32 v250, v129, v133
	v_mfma_f32_16x16x32_bf16 v[20:23], v[162:165], v[186:189], v[20:23]
	v_mfma_f32_16x16x32_bf16 v[16:19], v[166:169], v[182:185], v[16:19]
	v_cvt_pk_fp8_f32 v250, v129, v133 op_sel:[0,0,1]
	v_mfma_f32_16x16x32_bf16 v[16:19], v[170:173], v[186:189], v[16:19]
	v_mfma_f32_16x16x32_bf16 v[12:15], v[158:161], v[190:193], v[12:15]
	v_cvt_pk_fp8_f32 v251, v130, v134
	v_mfma_f32_16x16x32_bf16 v[12:15], v[162:165], v[194:197], v[12:15]
	v_bfi_b32 v152, s98, v204, v152
	v_mfma_f32_16x16x32_bf16 v[8:11], v[166:169], v[190:193], v[8:11]
	v_cvt_pk_fp8_f32 v251, v130, v134 op_sel:[0,0,1]
	v_mfma_f32_16x16x32_bf16 v[8:11], v[170:173], v[194:197], v[8:11]
	v_bfi_b32 v153, s98, v250, v153
	v_mfma_f32_16x16x32_bf16 v[4:7], v[158:161], v[234:237], v[4:7]
	v_cvt_pk_fp8_f32 v252, v131, v135
	v_mfma_f32_16x16x32_bf16 v[4:7], v[162:165], v[238:241], v[4:7]
	v_bfi_b32 v154, s98, v251, v154
	v_mfma_f32_16x16x32_bf16 v[0:3], v[166:169], v[234:237], v[0:3]
	v_cvt_pk_fp8_f32 v252, v131, v135 op_sel:[0,0,1]
	v_mfma_f32_16x16x32_bf16 v[0:3], v[170:173], v[238:241], v[0:3]
	v_bfi_b32 v155, s98, v252, v155
	s_setprio 0
	s_barrier
	s_bitcmp0_b32 s46, 0
	s_mov_b64 s[46:47], -1
	s_cbranch_scc0 .LBB0_345
	s_andn2_b64 vcc, exec, s[4:5]
	s_cbranch_vccnz .LBB0_345
	s_lshl_b32 s4, s67, 10
	s_lshl_b32 s5, s95, 8
	s_or_b32 s16, s4, s5
	s_and_b64 s[4:5], s[44:45], exec
	s_cselect_b32 s4, 8, 0
	v_lshlrev_b32_e32 v128, 3, v156
	s_or_b32 s4, s4, s16
	v_and_b32_e32 v128, 0xf0, v128
	v_or_b32_e32 v128, s4, v128
	v_or_b32_e32 v204, v128, v202
	v_lshlrev_b64 v[128:129], 12, v[204:205]
	v_lshl_add_u64 v[128:129], s[6:7], 0, v[128:129]
	s_lshl_b32 s36, s36, 7
	v_lshl_add_u64 v[128:129], v[128:129], 0, s[36:37]
	v_lshl_add_u64 v[128:129], v[128:129], 0, v[200:201]
	v_add_co_u32_e32 v130, vcc, 0x1000, v128
	global_store_dword v[128:129], v152, off
	s_nop 0
	v_addc_co_u32_e32 v131, vcc, 0, v129, vcc
	global_store_dword v[130:131], v153, off
	v_add_co_u32_e32 v130, vcc, 0x2000, v128
	s_nop 1
	v_addc_co_u32_e32 v131, vcc, 0, v129, vcc
	v_add_co_u32_e32 v128, vcc, 0x3000, v128
	global_store_dword v[130:131], v154, off
	s_nop 0
	v_addc_co_u32_e32 v129, vcc, 0, v129, vcc
	global_store_dword v[128:129], v155, off
	s_branch .LBB0_345
